# speedup vs baseline: 1.0073x; 1.0073x over previous
_Z13logits_kernelPKDv8_DF16bS1_PKfS3_PDv2_fS5_Pf:
	s_load_dwordx4 s[4:7], s[0:1], 0x0
	s_load_dwordx4 s[12:15], s[0:1], 0x10
	s_load_dwordx4 s[24:27], s[0:1], 0x20
	s_load_dwordx2 s[28:29], s[0:1], 0x30
	s_and_b32 s3, s2, 1
	s_lshl_b32 s3, s3, 3
	s_bfe_u32 s10, s2, 0x30003
	s_or_b32 s10, s10, s3
	s_bfe_u32 s3, s2, 0x20001
	s_lshl_b32 s3, s3, 2
	s_lshr_b32 s8, s2, 6
	s_or_b32 s3, s3, s8
	v_lshrrev_b32_e32 v1, 6, v0
	v_and_b32_e32 v2, 63, v0
	s_movk_i32 s11, 0x3000
	v_lshlrev_b32_e32 v2, 4, v2
	v_and_b32_e32 v5, 31, v0
	v_mad_u32_u24 v2, v1, s11, v2
	v_lshlrev_b32_e32 v5, 2, v5
	s_lshl_b32 s9, s3, 9
	v_add_u32_e32 v3, 0x1000, v2
	v_add_u32_e32 v4, 0x2000, v2
	v_add_u32_e32 v5, s9, v5
	s_mul_i32 s8, s10, 0xc000
	s_mul_i32 s9, s3, 0x30000
	s_waitcnt lgkmcnt(0)
	s_load_dword s22, s[14:15], 0x0
	global_load_dword v248, v5, s[12:13]
	global_load_dword v249, v5, s[12:13] offset:128
	global_load_dword v250, v5, s[12:13] offset:256
	global_load_dword v251, v5, s[12:13] offset:384
	s_add_u32 s4, s4, s8
	s_addc_u32 s5, s5, 0
	s_add_u32 s6, s6, s9
	s_addc_u32 s7, s7, 0
	s_add_u32 s16, s6, 0xc000
	s_addc_u32 s17, s7, 0
	s_add_u32 s18, s6, 0x18000
	s_addc_u32 s19, s7, 0
	s_add_u32 s20, s6, 0x24000
	s_addc_u32 s21, s7, 0
	global_load_dwordx4 v[8:11], v2, s[4:5]
	global_load_dwordx4 v[12:15], v2, s[4:5] offset:1024
	global_load_dwordx4 v[16:19], v2, s[4:5] offset:2048
	global_load_dwordx4 v[20:23], v2, s[4:5] offset:3072
	global_load_dwordx4 v[24:27], v3, s[4:5]
	global_load_dwordx4 v[28:31], v3, s[4:5] offset:1024
	global_load_dwordx4 v[32:35], v3, s[4:5] offset:2048
	global_load_dwordx4 v[36:39], v3, s[4:5] offset:3072
	global_load_dwordx4 v[40:43], v4, s[4:5]
	global_load_dwordx4 v[44:47], v4, s[4:5] offset:1024
	global_load_dwordx4 v[48:51], v4, s[4:5] offset:2048
	global_load_dwordx4 v[52:55], v4, s[4:5] offset:3072
	global_load_dwordx4 v[56:59], v2, s[6:7]
	global_load_dwordx4 v[104:107], v2, s[16:17]
	global_load_dwordx4 v[152:155], v2, s[18:19]
	global_load_dwordx4 v[200:203], v2, s[20:21]
	global_load_dwordx4 v[60:63], v2, s[6:7] offset:1024
	global_load_dwordx4 v[108:111], v2, s[16:17] offset:1024
	global_load_dwordx4 v[156:159], v2, s[18:19] offset:1024
	global_load_dwordx4 v[204:207], v2, s[20:21] offset:1024
	global_load_dwordx4 v[64:67], v2, s[6:7] offset:2048
	global_load_dwordx4 v[112:115], v2, s[16:17] offset:2048
	global_load_dwordx4 v[160:163], v2, s[18:19] offset:2048
	global_load_dwordx4 v[208:211], v2, s[20:21] offset:2048
	global_load_dwordx4 v[68:71], v2, s[6:7] offset:3072
	global_load_dwordx4 v[116:119], v2, s[16:17] offset:3072
	global_load_dwordx4 v[164:167], v2, s[18:19] offset:3072
	global_load_dwordx4 v[212:215], v2, s[20:21] offset:3072
	global_load_dwordx4 v[72:75], v3, s[6:7]
	global_load_dwordx4 v[120:123], v3, s[16:17]
	global_load_dwordx4 v[168:171], v3, s[18:19]
	global_load_dwordx4 v[216:219], v3, s[20:21]
	global_load_dwordx4 v[76:79], v3, s[6:7] offset:1024
	global_load_dwordx4 v[124:127], v3, s[16:17] offset:1024
	global_load_dwordx4 v[172:175], v3, s[18:19] offset:1024
	global_load_dwordx4 v[220:223], v3, s[20:21] offset:1024
	global_load_dwordx4 v[80:83], v3, s[6:7] offset:2048
	global_load_dwordx4 v[128:131], v3, s[16:17] offset:2048
	global_load_dwordx4 v[176:179], v3, s[18:19] offset:2048
	global_load_dwordx4 v[224:227], v3, s[20:21] offset:2048
	global_load_dwordx4 v[84:87], v3, s[6:7] offset:3072
	global_load_dwordx4 v[132:135], v3, s[16:17] offset:3072
	global_load_dwordx4 v[180:183], v3, s[18:19] offset:3072
	global_load_dwordx4 v[228:231], v3, s[20:21] offset:3072
	global_load_dwordx4 v[88:91], v4, s[6:7]
	global_load_dwordx4 v[136:139], v4, s[16:17]
	global_load_dwordx4 v[184:187], v4, s[18:19]
	global_load_dwordx4 v[232:235], v4, s[20:21]
	global_load_dwordx4 v[92:95], v4, s[6:7] offset:1024
	global_load_dwordx4 v[140:143], v4, s[16:17] offset:1024
	global_load_dwordx4 v[188:191], v4, s[18:19] offset:1024
	global_load_dwordx4 v[236:239], v4, s[20:21] offset:1024
	global_load_dwordx4 v[96:99], v4, s[6:7] offset:2048
	global_load_dwordx4 v[144:147], v4, s[16:17] offset:2048
	global_load_dwordx4 v[192:195], v4, s[18:19] offset:2048
	global_load_dwordx4 v[240:243], v4, s[20:21] offset:2048
	global_load_dwordx4 v[100:103], v4, s[6:7] offset:3072
	global_load_dwordx4 v[148:151], v4, s[16:17] offset:3072
	global_load_dwordx4 v[196:199], v4, s[18:19] offset:3072
	global_load_dwordx4 v[244:247], v4, s[20:21] offset:3072
	s_waitcnt vmcnt(47)
	v_mfma_f32_32x32x16_bf16 a[0:15], v[8:11], v[56:59], 0
	s_waitcnt vmcnt(46)
	v_mfma_f32_32x32x16_bf16 a[0:15], v[8:11], v[104:107], a[0:15]
	s_waitcnt vmcnt(45)
	v_mfma_f32_32x32x16_bf16 a[0:15], v[8:11], v[152:155], a[0:15]
	s_waitcnt vmcnt(44)
	v_mfma_f32_32x32x16_bf16 a[0:15], v[8:11], v[200:203], a[0:15]
	s_waitcnt vmcnt(43)
	v_mfma_f32_32x32x16_bf16 a[0:15], v[12:15], v[60:63], a[0:15]
	s_waitcnt vmcnt(42)
	v_mfma_f32_32x32x16_bf16 a[0:15], v[12:15], v[108:111], a[0:15]
	s_waitcnt vmcnt(41)
	v_mfma_f32_32x32x16_bf16 a[0:15], v[12:15], v[156:159], a[0:15]
	s_waitcnt vmcnt(40)
	v_mfma_f32_32x32x16_bf16 a[0:15], v[12:15], v[204:207], a[0:15]
	s_waitcnt vmcnt(39)
	v_mfma_f32_32x32x16_bf16 a[0:15], v[16:19], v[64:67], a[0:15]
	s_waitcnt vmcnt(38)
	v_mfma_f32_32x32x16_bf16 a[0:15], v[16:19], v[112:115], a[0:15]
	s_waitcnt vmcnt(37)
	v_mfma_f32_32x32x16_bf16 a[0:15], v[16:19], v[160:163], a[0:15]
	s_waitcnt vmcnt(36)
	v_mfma_f32_32x32x16_bf16 a[0:15], v[16:19], v[208:211], a[0:15]
	s_waitcnt vmcnt(35)
	v_mfma_f32_32x32x16_bf16 a[0:15], v[20:23], v[68:71], a[0:15]
	s_waitcnt vmcnt(34)
	v_mfma_f32_32x32x16_bf16 a[0:15], v[20:23], v[116:119], a[0:15]
	s_waitcnt vmcnt(33)
	v_mfma_f32_32x32x16_bf16 a[0:15], v[20:23], v[164:167], a[0:15]
	s_waitcnt vmcnt(32)
	v_mfma_f32_32x32x16_bf16 a[0:15], v[20:23], v[212:215], a[0:15]
	s_waitcnt vmcnt(31)
	v_mfma_f32_32x32x16_bf16 a[0:15], v[24:27], v[72:75], a[0:15]
	s_waitcnt vmcnt(30)
	v_mfma_f32_32x32x16_bf16 a[0:15], v[24:27], v[120:123], a[0:15]
	s_waitcnt vmcnt(29)
	v_mfma_f32_32x32x16_bf16 a[0:15], v[24:27], v[168:171], a[0:15]
	s_waitcnt vmcnt(28)
	v_mfma_f32_32x32x16_bf16 a[0:15], v[24:27], v[216:219], a[0:15]
	s_waitcnt vmcnt(27)
	v_mfma_f32_32x32x16_bf16 a[0:15], v[28:31], v[76:79], a[0:15]
	s_waitcnt vmcnt(26)
	v_mfma_f32_32x32x16_bf16 a[0:15], v[28:31], v[124:127], a[0:15]
	s_waitcnt vmcnt(25)
	v_mfma_f32_32x32x16_bf16 a[0:15], v[28:31], v[172:175], a[0:15]
	s_waitcnt vmcnt(24)
	v_mfma_f32_32x32x16_bf16 a[0:15], v[28:31], v[220:223], a[0:15]
	s_waitcnt vmcnt(23)
	v_mfma_f32_32x32x16_bf16 a[0:15], v[32:35], v[80:83], a[0:15]
	s_waitcnt vmcnt(22)
	v_mfma_f32_32x32x16_bf16 a[0:15], v[32:35], v[128:131], a[0:15]
	s_waitcnt vmcnt(21)
	v_mfma_f32_32x32x16_bf16 a[0:15], v[32:35], v[176:179], a[0:15]
	s_waitcnt vmcnt(20)
	v_mfma_f32_32x32x16_bf16 a[0:15], v[32:35], v[224:227], a[0:15]
	s_waitcnt vmcnt(19)
	v_mfma_f32_32x32x16_bf16 a[0:15], v[36:39], v[84:87], a[0:15]
	s_waitcnt vmcnt(18)
	v_mfma_f32_32x32x16_bf16 a[0:15], v[36:39], v[132:135], a[0:15]
	s_waitcnt vmcnt(17)
	v_mfma_f32_32x32x16_bf16 a[0:15], v[36:39], v[180:183], a[0:15]
	s_waitcnt vmcnt(16)
	v_mfma_f32_32x32x16_bf16 a[0:15], v[36:39], v[228:231], a[0:15]
	s_waitcnt vmcnt(15)
	v_mfma_f32_32x32x16_bf16 a[0:15], v[40:43], v[88:91], a[0:15]
	s_waitcnt vmcnt(14)
	v_mfma_f32_32x32x16_bf16 a[0:15], v[40:43], v[136:139], a[0:15]
	s_waitcnt vmcnt(13)
	v_mfma_f32_32x32x16_bf16 a[0:15], v[40:43], v[184:187], a[0:15]
	s_waitcnt vmcnt(12)
	v_mfma_f32_32x32x16_bf16 a[0:15], v[40:43], v[232:235], a[0:15]
	s_waitcnt vmcnt(11)
	v_mfma_f32_32x32x16_bf16 a[0:15], v[44:47], v[92:95], a[0:15]
	s_waitcnt vmcnt(10)
	v_mfma_f32_32x32x16_bf16 a[0:15], v[44:47], v[140:143], a[0:15]
	s_waitcnt vmcnt(9)
	v_mfma_f32_32x32x16_bf16 a[0:15], v[44:47], v[188:191], a[0:15]
	s_waitcnt vmcnt(8)
	v_mfma_f32_32x32x16_bf16 a[0:15], v[44:47], v[236:239], a[0:15]
	v_add_f32_e32 v8, 0, v248
	v_add_f32_e32 v8, v8, v249
	v_add_f32_e32 v8, v8, v250
	v_add_f32_e32 v8, v8, v251
	v_mov_b32_e32 v9, 0x3fb8aa3b
	s_waitcnt lgkmcnt(0)
	v_mul_f32_e32 v9, s22, v9
	v_exp_f32_e32 v9, v9
	v_add_f32_e32 v10, 0x2b8cbccc, v8
	v_div_scale_f32 v11, s[8:9], v10, v10, v9
	v_rcp_f32_e32 v12, v11
	v_div_scale_f32 v13, vcc, v9, v10, v9
	v_fma_f32 v14, -v11, v12, 1.0
	v_fmac_f32_e32 v12, v14, v12
	v_mul_f32_e32 v14, v13, v12
	v_fma_f32 v15, -v11, v14, v13
	v_fmac_f32_e32 v14, v15, v12
	v_fma_f32 v11, -v11, v14, v13
	v_div_fmas_f32 v11, v11, v12, v14
	v_div_fixup_f32 v9, v11, v10, v9
	v_lshlrev_b32_e32 v10, 2, v0
	v_add_u32_e32 v10, 0x4000, v10
	v_cmp_gt_u32_e32 vcc, 32, v0
	s_and_saveexec_b64 s[8:9], vcc
	ds_write2_b32 v10, v8, v9 offset0:128 offset1:160
	s_mov_b64 exec, s[8:9]
	s_waitcnt vmcnt(7)
	v_mfma_f32_32x32x16_bf16 a[0:15], v[48:51], v[96:99], a[0:15]
	s_waitcnt vmcnt(6)
	v_mfma_f32_32x32x16_bf16 a[0:15], v[48:51], v[144:147], a[0:15]
	s_waitcnt vmcnt(5)
	v_mfma_f32_32x32x16_bf16 a[0:15], v[48:51], v[192:195], a[0:15]
	s_waitcnt vmcnt(4)
	v_mfma_f32_32x32x16_bf16 a[0:15], v[48:51], v[240:243], a[0:15]
	v_mul_u32_u24_e32 v1, 0x1080, v1
	s_movk_i32 s4, 0x7f
	s_movk_i32 s6, 0x84
	v_cmp_lt_u32_e32 vcc, s4, v0
	v_lshrrev_b32_e32 v11, 3, v0
	v_and_b32_e32 v10, 31, v0
	v_and_b32_e32 v11, 4, v11
	v_mul_u32_u24_e32 v11, 0x84, v11
	v_lshlrev_b32_e32 v9, 2, v10
	v_bfe_u32 v6, v0, 2, 5
	v_and_b32_e32 v7, 3, v0
	v_add3_u32 v1, v1, v11, v9
	v_lshlrev_b32_e32 v8, 3, v7
	s_waitcnt vmcnt(3)
	v_mfma_f32_32x32x16_bf16 a[0:15], v[52:55], v[100:103], a[0:15]
	s_waitcnt vmcnt(2)
	v_mfma_f32_32x32x16_bf16 a[0:15], v[52:55], v[148:151], a[0:15]
	s_waitcnt vmcnt(1)
	v_mfma_f32_32x32x16_bf16 a[0:15], v[52:55], v[196:199], a[0:15]
	s_waitcnt vmcnt(0)
	v_mfma_f32_32x32x16_bf16 a[0:15], v[52:55], v[244:247], a[0:15]
	s_nop 11
	ds_write_b32 v1, a0
	ds_write_b32 v1, a1 offset:132
	ds_write_b32 v1, a2 offset:264
	ds_write_b32 v1, a3 offset:396
	ds_write_b32 v1, a4 offset:1056
	ds_write_b32 v1, a5 offset:1188
	ds_write_b32 v1, a6 offset:1320
	ds_write_b32 v1, a7 offset:1452
	ds_write_b32 v1, a8 offset:2112
	ds_write_b32 v1, a9 offset:2244
	ds_write_b32 v1, a10 offset:2376
	ds_write_b32 v1, a11 offset:2508
	ds_write_b32 v1, a12 offset:3168
	ds_write_b32 v1, a13 offset:3300
	ds_write_b32 v1, a14 offset:3432
	ds_write_b32 v1, a15 offset:3564
	v_bfe_u32 v6, v0, 2, 5
	v_and_b32_e32 v7, 3, v0
	v_lshlrev_b32_e32 v9, 3, v7
	v_readfirstlane_b32 s30, v0
	v_sub_u32_e32 v10, v6, v9
	s_waitcnt lgkmcnt(0)
	s_barrier
	s_cmpk_ge_u32 s30, 0x80
	s_cbranch_scc1 .Llg_k1
	v_mul_u32_u24_e32 v2, 0x84, v6
	v_lshlrev_b32_e32 v8, 5, v7
	v_add_u32_e32 v2, v2, v8
	v_add_u32_e32 v8, 0x4280, v8
	v_add_u32_e32 v3, 0x1080, v2
	v_add_u32_e32 v4, 0x2100, v2
	v_add_u32_e32 v5, 0x3180, v2
	ds_read_b128 v[48:51], v8
	ds_read_b128 v[52:55], v8 offset:16
	ds_read2_b32 v[16:17], v2 offset0:0 offset1:1
	ds_read2_b32 v[18:19], v2 offset0:2 offset1:3
	ds_read2_b32 v[20:21], v2 offset0:4 offset1:5
	ds_read2_b32 v[22:23], v2 offset0:6 offset1:7
	ds_read2_b32 v[24:25], v3 offset0:0 offset1:1
	ds_read2_b32 v[26:27], v3 offset0:2 offset1:3
	ds_read2_b32 v[28:29], v3 offset0:4 offset1:5
	ds_read2_b32 v[30:31], v3 offset0:6 offset1:7
	ds_read2_b32 v[32:33], v4 offset0:0 offset1:1
	ds_read2_b32 v[34:35], v4 offset0:2 offset1:3
	ds_read2_b32 v[36:37], v4 offset0:4 offset1:5
	ds_read2_b32 v[38:39], v4 offset0:6 offset1:7
	s_waitcnt lgkmcnt(4)
	ds_read2_b32 v[40:41], v5 offset0:0 offset1:1
	ds_read2_b32 v[42:43], v5 offset0:2 offset1:3
	ds_read2_b32 v[44:45], v5 offset0:4 offset1:5
	ds_read2_b32 v[46:47], v5 offset0:6 offset1:7
	s_waitcnt lgkmcnt(0)
	s_branch .Llg_join
